# redundant per-tile feat loads removed: MP0 waves 1-7 branch around the two feat loads only wave 0 consumes; node kernel drops its dead second feat load and loads the first on wave 0 only
# speedup vs baseline: 1.0047x; 1.0047x over previous
.LBB5_14:
	v_or_b32_e32 v0, s33, v200
	ds_read_b128 v[142:145], v0 offset:0
	s_waitcnt lgkmcnt(4)
	s_nop 0
	v_mfma_f32_16x16x32_f16 v[134:137], v[114:117], v[134:137], v[166:169]
	ds_read_b128 v[146:149], v0 offset:0x1000
	s_waitcnt lgkmcnt(4)
	s_nop 0
	v_mfma_f32_16x16x32_f16 v[138:141], v[114:117], v[138:141], v[170:173]
	ds_read_b128 v[150:153], v0 offset:0x2000
	s_waitcnt lgkmcnt(4)
	s_nop 0
	v_mfma_f32_16x16x32_f16 v[154:157], v[114:117], v[158:161], v[174:177]
	ds_read_b128 v[158:161], v0 offset:0x3000
	s_waitcnt lgkmcnt(4)
	s_nop 0
	v_mfma_f32_16x16x32_f16 v[162:165], v[114:117], v[162:165], v[178:181]
	ds_read_b128 v[166:169], v205 offset:0
	s_waitcnt lgkmcnt(4)
	s_nop 0
	v_mfma_f32_16x16x32_f16 v[134:137], v[106:109], v[142:145], v[134:137]
	ds_read_b128 v[142:145], v205 offset:0x100
	s_waitcnt lgkmcnt(4)
	s_nop 0
	v_mfma_f32_16x16x32_f16 v[138:141], v[106:109], v[146:149], v[138:141]
	ds_read_b128 v[146:149], v205 offset:0x200
	s_waitcnt lgkmcnt(4)
	s_nop 0
	v_mfma_f32_16x16x32_f16 v[150:153], v[106:109], v[150:153], v[154:157]
	ds_read_b128 v[154:157], v205 offset:0x300
	s_waitcnt lgkmcnt(4)
	s_nop 0
	v_mfma_f32_16x16x32_f16 v[158:161], v[106:109], v[158:161], v[162:165]
	s_waitcnt lgkmcnt(3)
	s_nop 0
	v_mfma_f32_16x16x32_f16 v[134:137], v[102:105], v[166:169], v[134:137]
	s_waitcnt lgkmcnt(2)
	s_nop 0
	v_mfma_f32_16x16x32_f16 v[138:141], v[102:105], v[142:145], v[138:141]
	s_waitcnt lgkmcnt(1)
	s_nop 0
	v_mfma_f32_16x16x32_f16 v[142:145], v[102:105], v[146:149], v[150:153]
	s_waitcnt lgkmcnt(0)
	s_nop 0
	v_mfma_f32_16x16x32_f16 v[146:149], v[102:105], v[154:157], v[158:161]
	s_nop 1
	v_cvt_pk_f16_f32 v1, v136, v137
	v_pk_max_f16 v1, v1, 0
	v_cvt_pk_f16_f32 v0, v134, v135
	v_pk_max_f16 v0, v0, 0
	v_cvt_pk_f16_f32 v135, v140, v141
	v_pk_max_f16 v135, v135, 0
	v_cvt_pk_f16_f32 v134, v138, v139
	v_pk_max_f16 v134, v134, 0
	ds_write2st64_b64 v218, v[0:1], v[134:135] offset1:8
	v_cvt_pk_f16_f32 v1, v144, v145
	v_pk_max_f16 v1, v1, 0
	v_cvt_pk_f16_f32 v0, v142, v143
	v_pk_max_f16 v0, v0, 0
	s_lshl_b32 s34, s2, 14
	v_cvt_pk_f16_f32 v135, v148, v149
	v_pk_max_f16 v135, v135, 0
	v_cvt_pk_f16_f32 v134, v146, v147
	v_pk_max_f16 v134, v134, 0
	s_or_b32 s34, s34, 0x18000
	ds_write2st64_b64 v218, v[0:1], v[134:135] offset0:16 offset1:24
	v_or_b32_e32 v172, s34, v197
	v_or_b32_e32 v223, s34, v198
	v_or_b32_e32 v143, s34, v199
	v_or_b32_e32 v142, s34, v200
	v_add_u32_e32 v0, s34, v208
	s_xor_b32 s34, s2, 1
	s_waitcnt vmcnt(2) lgkmcnt(0)
	s_barrier
	ds_read_b128 v[134:137], v201 offset:0
	s_mul_i32 s37, s34, 0xc000
	ds_read_b128 v[138:141], v202 offset:0
	ds_read_b128 v[144:147], v203 offset:0
	ds_read_b128 v[148:151], v204 offset:0
	v_add_u32_e32 v1, s37, v209
	ds_read_b128 v[152:155], v1 offset:0
	ds_read_b128 v[156:159], v1 offset:0x4000
	ds_read_b128 v[160:163], v1 offset:0x8000
	ds_read_b128 v[164:167], v1 offset:0x400
	ds_read_b128 v[168:171], v1 offset:0x4400
	ds_read_b128 v[174:177], v1 offset:0x8400
	ds_read_b128 v[178:181], v172 offset:0
	s_waitcnt lgkmcnt(10)
	v_subrev_u32_e32 v186, 56, v215
	v_mfma_f32_16x16x32_f16 v[182:185], v[2:5], v[134:137], v[118:121]
	v_min_u32_e32 v225, s17, v186
	v_add_u32_e32 v224, s20, v216
	v_mov_b32_e32 v230, s16
	v_mfma_f32_16x16x32_f16 v[186:189], v[42:45], v[134:137], v[122:125]
	v_cmp_gt_u32_e32 vcc, s8, v224
	ds_read_b128 v[226:229], v223 offset:0
	s_waitcnt lgkmcnt(10)
	v_mfma_f32_16x16x32_f16 v[134:137], v[66:69], v[134:137], v[126:129]
	v_lshl_or_b32 v173, v196, 8, v190
	v_cndmask_b32_e32 v230, v230, v224, vcc
	v_lshlrev_b32_e32 v234, 5, v230
	v_mfma_f32_16x16x32_f16 v[182:185], v[6:9], v[138:141], v[182:185]
	v_add_u32_e32 v196, -8, v215
	v_min_u32_e32 v238, s17, v196
	v_subrev_u32_e32 v196, 52, v215
	v_mfma_f32_16x16x32_f16 v[186:189], v[46:49], v[138:141], v[186:189]
	v_add_u32_e32 v221, -4, v215
	v_min_u32_e32 v196, s18, v196
	v_min_u32_e32 v221, s18, v221
	v_mfma_f32_16x16x32_f16 v[230:233], v[70:73], v[138:141], v[134:137]
	s_cmp_lg_u32 s42, 0
	s_cbranch_scc1 .Lmp0_nofeat
	global_load_dwordx4 v[134:137], v234, s[6:7]
	global_load_dwordx4 v[138:141], v234, s[6:7] offset:16
.Lmp0_nofeat:
	ds_read_b128 v[234:237], v143 offset:0
	s_waitcnt lgkmcnt(10)
	v_lshl_or_b32 v242, v192, 8, v190
	v_mfma_f32_16x16x32_f16 v[182:185], v[50:53], v[144:147], v[182:185]
	global_load_dword v192, v196, s[4:5]
	v_subrev_u32_e32 v239, 48, v215
	global_load_dword v221, v221, s[4:5]
	v_mfma_f32_16x16x32_f16 v[186:189], v[18:21], v[144:147], v[186:189]
	v_min_u32_e32 v222, s19, v215
	v_min_u32_e32 v239, s19, v239
	v_lshl_or_b32 v241, v194, 8, v191
	v_mfma_f32_16x16x32_f16 v[144:147], v[74:77], v[144:147], v[230:233]
	global_load_dword v196, v239, s[4:5]
	ds_read_b128 v[230:233], v142 offset:0
	s_waitcnt lgkmcnt(10)
	global_load_dword v194, v222, s[4:5]
	s_add_i32 s2, s28, s3
	v_mfma_f32_16x16x32_f16 v[182:185], v[10:13], v[148:151], v[182:185]
	v_lshl_or_b32 v243, v193, 8, v190
	global_load_dword v193, v225, s[4:5]
	s_min_i32 s35, s2, s14
	v_mfma_f32_16x16x32_f16 v[186:189], v[58:61], v[148:151], v[186:189]
	global_load_dword v222, v238, s[4:5]
	s_lshl_b32 s35, s35, 14
	s_lshl_b32 s34, s34, 14
	v_mfma_f32_16x16x32_f16 v[148:151], v[90:93], v[148:151], v[144:147]
	s_add_i32 s36, s33, 0
	v_add_u32_e32 v1, s35, v210
	s_add_i32 s38, s25, s34
	s_add_i32 s39, s36, s21
	s_add_i32 s40, s26, s34
	s_add_i32 s34, s36, s23
	s_add_i32 m0, s39, 0x8000
	v_add_u32_e32 v240, s35, v211
	s_add_i32 s41, s34, 0x8000
	s_add_i32 s35, s39, 0x4000
	s_add_i32 s36, s22, s33
	v_add_u32_e32 v239, s37, v212
	ds_read_b128 v[144:147], v201 offset:0x1000
	s_waitcnt lgkmcnt(4)
	s_waitcnt lgkmcnt(5)
	s_nop 0
	v_pk_add_f16 v152, v152, v156
	v_pk_add_f16 v153, v153, v157
	v_pk_add_f16 v154, v154, v158
	v_pk_add_f16 v155, v155, v159
	v_pk_add_f16 v154, v154, v162
	v_pk_add_f16 v155, v155, v163
	v_pk_add_f16 v153, v153, v161
	v_pk_add_f16 v152, v152, v160
	ds_write_b128 v239, v[152:155]
	v_pk_add_f16 v152, v164, v168
	v_pk_add_f16 v153, v165, v169
	v_pk_add_f16 v154, v166, v170
	v_pk_add_f16 v155, v167, v171
	v_pk_add_f16 v154, v154, v176
	v_pk_add_f16 v155, v155, v177
	v_pk_add_f16 v153, v153, v175
	v_pk_add_f16 v152, v152, v174
	ds_write_b128 v239, v[152:155] offset:1024
	ds_read_b128 v[152:155], v202 offset:0x1000
	s_waitcnt lgkmcnt(4)
	global_load_lds_dwordx4 v173, s[12:13]
	s_mov_b32 m0, s38
	ds_read_b128 v[168:171], v203 offset:0x1000
	s_waitcnt lgkmcnt(4)
	v_mfma_f32_16x16x32_f16 v[182:185], v[14:17], v[178:181], v[182:185]
	global_load_lds_dwordx4 v1, s[12:13]
	ds_read_b128 v[174:177], v204 offset:0x1000
	v_mfma_f32_16x16x32_f16 v[186:189], v[22:25], v[178:181], v[186:189]
	s_waitcnt lgkmcnt(4)
	v_mfma_f32_16x16x32_f16 v[178:181], v[86:89], v[178:181], v[130:133]
	v_mfma_f32_16x16x32_f16 v[156:159], v[26:29], v[226:229], v[182:185]
	v_mfma_f32_16x16x32_f16 v[160:163], v[34:37], v[226:229], v[186:189]
	v_mfma_f32_16x16x32_f16 v[164:167], v[78:81], v[226:229], v[178:181]
	v_mfma_f32_16x16x32_f16 v[156:159], v[30:33], v[234:237], v[156:159]
	v_mfma_f32_16x16x32_f16 v[160:163], v[38:41], v[234:237], v[160:163]
	v_mfma_f32_16x16x32_f16 v[164:167], v[82:85], v[234:237], v[164:167]
	v_mfma_f32_16x16x32_f16 v[156:159], v[54:57], v[230:233], v[156:159]
	v_mfma_f32_16x16x32_f16 v[160:163], v[62:65], v[230:233], v[160:163]
	v_mfma_f32_16x16x32_f16 v[164:167], v[94:97], v[230:233], v[164:167]
	s_mov_b32 m0, s41
	ds_read_b64 v[234:235], v0 offset:0
	ds_read_b128 v[178:181], v172 offset:0x1000
	s_waitcnt lgkmcnt(5)
	ds_read_b128 v[186:189], v223 offset:0x1000
	s_waitcnt lgkmcnt(5)
	s_nop 4
	v_exp_f32_e32 v1, v156
	s_waitcnt lgkmcnt(2)
	ds_read_b128 v[230:233], v143 offset:0x1000
	s_waitcnt lgkmcnt(5)
	global_load_lds_dwordx4 v241, s[12:13]
	v_add_f32_e32 v1, 1.0, v1
	v_rcp_f32_e32 v1, v1
	v_exp_f32_e32 v156, v160
	v_mfma_f32_16x16x32_f16 v[182:185], v[2:5], v[144:147], v[118:121]
	v_add_u32_e32 v225, v206, v213
	v_fma_f32 v1, v1, v164, v148
	v_exp_f32_e32 v1, v1
	v_add_f32_e32 v148, 1.0, v156
	v_exp_f32_e32 v156, v157
	v_rcp_f32_e32 v148, v148
	v_add_f32_e32 v1, 1.0, v1
	v_rcp_f32_e32 v1, v1
	v_add_f32_e32 v156, 1.0, v156
	v_rcp_f32_e32 v156, v156
	v_mfma_f32_16x16x32_f16 v[226:229], v[42:45], v[144:147], v[122:125]
	v_fma_f32 v1, v1, -2.0, 1.0
	v_fma_f32 v1, -v148, v1, v1
	v_fma_mixlo_f16 v1, v148, v234, v1 op_sel_hi:[0,1,0]
	v_mfma_f32_16x16x32_f16 v[144:147], v[66:69], v[144:147], v[126:129]
	v_exp_f32_e32 v148, v161
	v_fma_f32 v149, v156, v165, v149
	v_exp_f32_e32 v149, v149
	v_mfma_f32_16x16x32_f16 v[182:185], v[6:9], v[152:155], v[182:185]
	v_add_f32_e32 v148, 1.0, v148
	v_rcp_f32_e32 v156, v148
	v_add_f32_e32 v148, 1.0, v149
	v_mfma_f32_16x16x32_f16 v[226:229], v[46:49], v[152:155], v[226:229]
	v_rcp_f32_e32 v157, v148
	v_add_u32_e32 v173, 0x1000, v225
	v_mfma_f32_16x16x32_f16 v[144:147], v[70:73], v[152:155], v[144:147]
	v_mfma_f32_16x16x32_f16 v[152:155], v[50:53], v[168:171], v[182:185]
	v_mfma_f32_16x16x32_f16 v[182:185], v[18:21], v[168:171], v[226:229]
	v_mfma_f32_16x16x32_f16 v[144:147], v[74:77], v[168:171], v[144:147]
	ds_read_b128 v[168:171], v142 offset:0x1000
	s_waitcnt lgkmcnt(5)
	s_nop 0
	v_mfma_f32_16x16x32_f16 v[152:155], v[10:13], v[174:177], v[152:155]
	v_mfma_f32_16x16x32_f16 v[182:185], v[58:61], v[174:177], v[182:185]
	v_mfma_f32_16x16x32_f16 v[146:149], v[90:93], v[174:177], v[144:147]
	s_nop 3
	v_fma_f32 v144, v157, -2.0, 1.0
	v_fma_f32 v144, -v156, v144, v144
	v_fma_mixlo_f16 v144, v156, v234, v144 op_sel:[0,1,0] op_sel_hi:[0,1,0]
	s_mov_b32 m0, s40
	ds_read_b128 v[174:177], v201 offset:0x2000
	s_waitcnt lgkmcnt(4)
	ds_read_b128 v[226:229], v202 offset:0x2000
	s_waitcnt lgkmcnt(4)
	v_exp_f32_e32 v145, v158
	global_load_lds_dwordx4 v240, s[12:13]
	v_exp_f32_e32 v156, v162
	v_add_f32_e32 v145, 1.0, v145
	v_rcp_f32_e32 v145, v145
	v_mfma_f32_16x16x32_f16 v[152:155], v[14:17], v[178:181], v[152:155]
	v_pack_b32_f16 v144, v1, v144
	v_fma_f32 v145, v145, v166, v150
	v_add_f32_e32 v150, 1.0, v156
	v_rcp_f32_e32 v234, v150
	v_exp_f32_e32 v150, v159
	v_mfma_f32_16x16x32_f16 v[182:185], v[22:25], v[178:181], v[182:185]
	v_exp_f32_e32 v145, v145
	v_add_f32_e32 v150, 1.0, v150
	v_mfma_f32_16x16x32_f16 v[178:181], v[86:89], v[178:181], v[130:133]
	v_rcp_f32_e32 v150, v150
	v_add_f32_e32 v145, 1.0, v145
	v_rcp_f32_e32 v145, v145
	v_mfma_f32_16x16x32_f16 v[182:185], v[34:37], v[186:189], v[182:185]
	v_fmac_f32_e32 v151, v150, v167
	v_fma_f32 v145, v145, -2.0, 1.0
	v_mfma_f32_16x16x32_f16 v[178:181], v[78:81], v[186:189], v[178:181]
	v_fma_f32 v145, -v234, v145, v145
	v_fma_mixlo_f16 v145, v234, v235, v145 op_sel_hi:[0,1,0]
	v_mfma_f32_16x16x32_f16 v[152:155], v[26:29], v[186:189], v[152:155]
	ds_read_b128 v[186:189], v203 offset:0x2000
	s_waitcnt lgkmcnt(4)
	ds_read_b128 v[164:167], v204 offset:0x2000
	s_waitcnt lgkmcnt(4)
	s_nop 0
	v_mfma_f32_16x16x32_f16 v[156:159], v[38:41], v[230:233], v[182:185]
	s_nop 2
	v_exp_f32_e32 v182, v163
	v_mfma_f32_16x16x32_f16 v[160:163], v[82:85], v[230:233], v[178:181]
	s_nop 2
	v_exp_f32_e32 v178, v151
	v_mfma_f32_16x16x32_f16 v[152:155], v[30:33], v[230:233], v[152:155]
	v_add_f32_e32 v179, 1.0, v182
	v_add_f32_e32 v178, 1.0, v178
	v_mfma_f32_16x16x32_f16 v[150:153], v[54:57], v[168:171], v[152:155]
	v_mfma_f32_16x16x32_f16 v[154:157], v[62:65], v[168:171], v[156:159]
	s_nop 2
	v_rcp_f32_e32 v158, v178
	v_rcp_f32_e32 v159, v179
	v_mfma_f32_16x16x32_f16 v[168:171], v[94:97], v[168:171], v[160:163]
	v_fma_f32 v158, v158, -2.0, 1.0
	v_fma_f32 v158, -v159, v158, v158
	v_fma_mixlo_f16 v158, v159, v235, v158 op_sel:[0,1,0] op_sel_hi:[0,1,0]
	s_nop 0
	v_pack_b32_f16 v145, v145, v158
	global_store_dwordx2 v173, v[144:145], s[0:1] nt
	s_mov_b32 m0, s36
	ds_read_b64 v[238:239], v0 offset:0x1000
	ds_read_b128 v[178:181], v172 offset:0x2000
	s_waitcnt lgkmcnt(5)
	ds_read_b128 v[182:185], v223 offset:0x2000
	s_waitcnt lgkmcnt(5)
	v_exp_f32_e32 v1, v150
	s_waitcnt lgkmcnt(2)
	ds_read_b128 v[234:237], v143 offset:0x2000
	s_waitcnt lgkmcnt(5)
	global_load_lds_dwordx4 v243, s[12:13]
	v_add_f32_e32 v1, 1.0, v1
	v_rcp_f32_e32 v1, v1
	v_exp_f32_e32 v145, v151
	v_mfma_f32_16x16x32_f16 v[158:161], v[2:5], v[174:177], v[118:121]
	v_exp_f32_e32 v144, v154
	v_fma_f32 v1, v1, v168, v146
	v_exp_f32_e32 v1, v1
	v_mfma_f32_16x16x32_f16 v[230:233], v[42:45], v[174:177], v[122:125]
	v_add_f32_e32 v145, 1.0, v145
	v_rcp_f32_e32 v145, v145
	v_add_f32_e32 v1, 1.0, v1
	v_mfma_f32_16x16x32_f16 v[174:177], v[66:69], v[174:177], v[126:129]
	v_add_f32_e32 v144, 1.0, v144
	v_rcp_f32_e32 v1, v1
	v_rcp_f32_e32 v144, v144
	v_mfma_f32_16x16x32_f16 v[158:161], v[6:9], v[226:229], v[158:161]
	v_fma_f32 v145, v145, v169, v147
	v_exp_f32_e32 v145, v145
	v_exp_f32_e32 v146, v155
	v_mfma_f32_16x16x32_f16 v[174:177], v[70:73], v[226:229], v[174:177]
	v_fma_f32 v1, v1, -2.0, 1.0
	v_fma_f32 v1, -v144, v1, v1
	v_fma_mixlo_f16 v240, v144, v238, v1 op_sel_hi:[0,1,0]
	v_mfma_f32_16x16x32_f16 v[230:233], v[46:49], v[226:229], v[230:233]
	v_add_f32_e32 v144, 1.0, v145
	v_add_f32_e32 v1, 1.0, v146
	v_rcp_f32_e32 v150, v144
	v_mfma_f32_16x16x32_f16 v[158:161], v[50:53], v[186:189], v[158:161]
	v_rcp_f32_e32 v1, v1
	v_add_u32_e32 v173, 0x2000, v225
	v_fma_f32 v150, v150, -2.0, 1.0
	v_mfma_f32_16x16x32_f16 v[174:177], v[74:77], v[186:189], v[174:177]
	v_fma_f32 v243, -v1, v150, v150
	v_mfma_f32_16x16x32_f16 v[226:229], v[18:21], v[186:189], v[230:233]
	ds_read_b128 v[186:189], v142 offset:0x2000
	s_waitcnt lgkmcnt(5)
	s_nop 0
	v_mfma_f32_16x16x32_f16 v[158:161], v[10:13], v[164:167], v[158:161]
	v_mfma_f32_16x16x32_f16 v[144:147], v[90:93], v[164:167], v[174:177]
	v_mfma_f32_16x16x32_f16 v[226:229], v[58:61], v[164:167], v[226:229]
	s_mov_b32 m0, s35
	ds_read_b128 v[230:233], v201 offset:0x3000
	s_waitcnt lgkmcnt(4)
	v_exp_f32_e32 v150, v152
	v_mfma_f32_16x16x32_f16 v[164:167], v[14:17], v[178:181], v[158:161]
	ds_read_b128 v[160:163], v202 offset:0x3000
	s_waitcnt lgkmcnt(4)
	global_load_lds_dwordx4 v242, s[12:13]
	v_exp_f32_e32 v154, v153
	v_add_f32_e32 v150, 1.0, v150
	v_rcp_f32_e32 v150, v150
	v_mfma_f32_16x16x32_f16 v[174:177], v[22:25], v[178:181], v[226:229]
	v_add_f32_e32 v154, 1.0, v154
	v_rcp_f32_e32 v154, v154
	v_exp_f32_e32 v151, v156
	v_mfma_f32_16x16x32_f16 v[178:181], v[86:89], v[178:181], v[130:133]
	v_fma_f32 v148, v150, v170, v148
	v_exp_f32_e32 v148, v148
	v_fmac_f32_e32 v149, v154, v171
	v_mfma_f32_16x16x32_f16 v[226:229], v[26:29], v[182:185], v[164:167]
	v_exp_f32_e32 v149, v149
	v_add_f32_e32 v150, 1.0, v151
	v_rcp_f32_e32 v241, v150
	v_mfma_f32_16x16x32_f16 v[174:177], v[34:37], v[182:185], v[174:177]
	v_add_f32_e32 v148, 1.0, v148
	ds_read_b128 v[164:167], v203 offset:0x3000
	s_waitcnt lgkmcnt(4)
	v_mfma_f32_16x16x32_f16 v[178:181], v[78:81], v[182:185], v[178:181]
	v_exp_f32_e32 v155, v157
	v_rcp_f32_e32 v148, v148
	v_add_f32_e32 v149, 1.0, v149
	v_mfma_f32_16x16x32_f16 v[150:153], v[30:33], v[234:237], v[226:229]
	v_rcp_f32_e32 v149, v149
	ds_read_b128 v[168:171], v204 offset:0x3000
	s_waitcnt lgkmcnt(4)
	v_mfma_f32_16x16x32_f16 v[174:177], v[38:41], v[234:237], v[174:177]
	v_fma_f32 v148, v148, -2.0, 1.0
	v_fma_f32 v148, -v241, v148, v148
	v_fma_mixlo_f16 v241, v241, v239, v148 op_sel_hi:[0,1,0]
	v_mfma_f32_16x16x32_f16 v[178:181], v[82:85], v[234:237], v[178:181]
	v_fma_mixhi_f16 v240, v1, v238, v243 op_sel:[0,1,0] op_sel_hi:[0,1,0]
	v_mfma_f32_16x16x32_f16 v[156:159], v[54:57], v[186:189], v[150:153]
	s_nop 2
	v_add_f32_e32 v150, 1.0, v155
	v_mfma_f32_16x16x32_f16 v[152:155], v[62:65], v[186:189], v[174:177]
	s_nop 2
	v_rcp_f32_e32 v174, v150
	v_fma_f32 v175, v149, -2.0, 1.0
	v_mfma_f32_16x16x32_f16 v[148:151], v[94:97], v[186:189], v[178:181]
	v_fma_f32 v175, -v174, v175, v175
	v_fma_mixhi_f16 v241, v174, v239, v175 op_sel:[0,1,0] op_sel_hi:[0,1,0]
	global_store_dwordx2 v173, v[240:241], s[0:1] nt
	ds_read_b64 v[188:189], v0 offset:0x2000
	ds_read_b64 v[0:1], v0 offset:0x3000
	ds_read_b128 v[172:175], v172 offset:0x3000
	s_waitcnt lgkmcnt(6)
	s_andn2_b64 vcc, exec, s[10:11]
	v_mfma_f32_16x16x32_f16 v[180:183], v[2:5], v[230:233], v[118:121]
	s_waitcnt vmcnt(14)
	v_mfma_f32_16x16x32_f16 v[176:179], v[42:45], v[230:233], v[122:125]
	v_mfma_f32_16x16x32_f16 v[184:187], v[66:69], v[230:233], v[126:129]
	s_cbranch_vccnz .LBB5_11
	v_cvt_pk_f16_f32 v226, v134, v135
	v_cvt_pk_f16_f32 v227, v136, v137
	v_cvt_pk_f16_f32 v228, v138, v139
	v_cvt_pk_f16_f32 v229, v140, v141
	s_add_i32 s46, s20, s30
	s_add_i32 s46, s46, 63
	s_cmp_lt_i32 s46, s8
	s_cbranch_scc1 .Lmp0_fb_nomask
	v_cmp_gt_i32_e32 vcc, s8, v224
	s_nop 1
	v_cndmask_b32_e32 v226, 0, v226, vcc
	v_cndmask_b32_e32 v227, 0, v227, vcc
	v_cndmask_b32_e32 v228, 0, v228, vcc
	v_cndmask_b32_e32 v229, 0, v229, vcc

_Z10mp2_kernelILb0ELi2EEvPKDF16_PDF16_PKiPKfPKDv8_DF16_S6_S6_ii:
	s_load_dwordx2 s[4:5], s[0:1], 0x20
	v_readfirstlane_b32 s21, v0
	s_lshr_b32 s26, s21, 6
	s_lshr_b32 s22, s21, 6
	s_mul_i32 s3, s22, 5
	s_add_i32 s6, s3, 0xe8
	s_mov_b32 s7, 0
	s_lshl_b64 s[6:7], s[6:7], 10
	v_and_b32_e32 v30, 63, v0
	s_waitcnt lgkmcnt(0)
	s_add_u32 s4, s4, s6
	s_addc_u32 s5, s5, s7
	v_lshlrev_b32_e32 v28, 4, v30
	v_mov_b32_e32 v29, 0
	v_lshl_add_u64 v[14:15], s[4:5], 0, v[28:29]
	global_load_dwordx4 v[2:5], v28, s[4:5] offset:1024
	global_load_dwordx4 v[6:9], v28, s[4:5] offset:2048
	global_load_dwordx4 v[10:13], v28, s[4:5] offset:3072
	v_add_co_u32_e32 v22, vcc, 0x1000, v14
	s_nop 1
	v_addc_co_u32_e32 v23, vcc, 0, v15, vcc
	global_load_dwordx4 v[14:17], v28, s[4:5]
	global_load_dwordx4 v[18:21], v[22:23], off
	v_cmp_gt_u32_e32 vcc, 64, v0
	s_and_saveexec_b64 s[4:5], vcc
	s_cbranch_execnz .LBB8_3
	s_or_b64 exec, exec, s[4:5]
	s_load_dwordx2 s[12:13], s[0:1], 0x38
	s_waitcnt lgkmcnt(0)
	s_cmp_ge_i32 s2, s13
	s_cbranch_scc0 .LBB8_4

.LBB8_5:
	v_add_u32_e32 v22, s18, v47
	v_mov_b32_e32 v23, s14
	v_cmp_gt_u32_e32 vcc, s12, v22
	s_waitcnt lgkmcnt(0)
	s_barrier
	v_add_u32_e32 v56, -4, v46
	v_min_u32_e32 v56, s16, v56
	v_cndmask_b32_e32 v22, v23, v22, vcc
	v_lshlrev_b32_e32 v27, 4, v22
	s_cmp_lg_u32 s26, 0
	s_cbranch_scc1 .Lnode_nofeat
	global_load_dwordx4 v[22:25], v27, s[10:11]
.Lnode_nofeat:
	v_subrev_u32_e32 v27, 52, v46
	v_min_u32_e32 v27, s16, v27
	global_load_dword v27, v27, s[8:9]
	global_load_dword v92, v56, s[8:9]
	v_subrev_u32_e32 v56, 48, v46
	v_min_u32_e32 v56, s17, v56
	global_load_dword v93, v56, s[8:9]
	v_min_u32_e32 v56, s17, v46
	global_load_dword v94, v56, s[8:9]
	v_subrev_u32_e32 v56, 56, v46
	v_min_u32_e32 v56, s15, v56
	global_load_dword v95, v56, s[8:9]
	v_add_u32_e32 v56, -8, v46
	s_add_i32 s25, s24, s19
	v_min_u32_e32 v56, s15, v56
	global_load_dword v96, v56, s[8:9]
	v_lshl_or_b32 v50, v50, 8, v29
	s_add_i32 m0, s25, 0x4000
	s_add_i32 s24, s24, s20
	global_load_lds_dwordx4 v50, s[4:5]
	v_lshl_or_b32 v50, v51, 8, v31
	s_add_i32 m0, s24, 0x4000
	s_add_i32 s2, s2, s3
	global_load_lds_dwordx4 v50, s[4:5]
	v_or_b32_e32 v50, s23, v32
	v_or_b32_e32 v51, s23, v33
	v_or_b32_e32 v97, s23, v34
	v_or_b32_e32 v98, s23, v35
	ds_read_b128 v[56:59], v50 offset:0
	ds_read_b128 v[60:63], v50 offset:0x1000
	ds_read_b128 v[64:67], v50 offset:0x2000
	ds_read_b128 v[68:71], v50 offset:0x3000
	ds_read_b128 v[72:75], v51 offset:0
	s_nop 0
	s_waitcnt lgkmcnt(4)
	s_nop 0
	v_mfma_f32_16x16x32_f16 v[56:59], v[14:17], v[56:59], 0
	ds_read_b128 v[76:79], v51 offset:0x1000
	s_waitcnt lgkmcnt(4)
	s_nop 0
	v_mfma_f32_16x16x32_f16 v[60:63], v[14:17], v[60:63], 0
	ds_read_b128 v[80:83], v51 offset:0x2000
	s_waitcnt lgkmcnt(4)
	s_nop 0
	v_mfma_f32_16x16x32_f16 v[64:67], v[14:17], v[64:67], 0
	ds_read_b128 v[84:87], v51 offset:0x3000
	s_waitcnt lgkmcnt(4)
	s_nop 0
	v_mfma_f32_16x16x32_f16 v[68:71], v[14:17], v[68:71], 0
	ds_read_b128 v[88:91], v97 offset:0
	s_waitcnt lgkmcnt(4)
	s_nop 0
	v_mfma_f32_16x16x32_f16 v[56:59], v[2:5], v[72:75], v[56:59]
	ds_read_b128 v[72:75], v97 offset:0x1000
	s_waitcnt lgkmcnt(4)
	s_nop 0
	v_mfma_f32_16x16x32_f16 v[60:63], v[2:5], v[76:79], v[60:63]
	ds_read_b128 v[76:79], v97 offset:0x2000
	s_waitcnt lgkmcnt(4)
	s_nop 0
	v_mfma_f32_16x16x32_f16 v[64:67], v[2:5], v[80:83], v[64:67]
	ds_read_b128 v[80:83], v97 offset:0x3000
	s_waitcnt lgkmcnt(4)
	s_nop 0
	v_mfma_f32_16x16x32_f16 v[68:71], v[2:5], v[84:87], v[68:71]
	ds_read_b128 v[84:87], v98 offset:0
	s_waitcnt lgkmcnt(4)
	s_nop 0
	v_mfma_f32_16x16x32_f16 v[56:59], v[6:9], v[88:91], v[56:59]
	ds_read_b128 v[88:91], v98 offset:0x1000
	s_waitcnt lgkmcnt(4)
	s_nop 0
	v_mfma_f32_16x16x32_f16 v[60:63], v[6:9], v[72:75], v[60:63]
	ds_read_b128 v[72:75], v98 offset:0x2000
	s_waitcnt lgkmcnt(4)
	s_nop 0
	v_mfma_f32_16x16x32_f16 v[64:67], v[6:9], v[76:79], v[64:67]
	ds_read_b128 v[76:79], v98 offset:0x3000
	s_waitcnt lgkmcnt(4)
	s_nop 0
	v_mfma_f32_16x16x32_f16 v[68:71], v[6:9], v[80:83], v[68:71]
	ds_read_b128 v[80:83], v37 offset:0
	s_waitcnt lgkmcnt(4)
	s_nop 0
	v_mfma_f32_16x16x32_f16 v[56:59], v[10:13], v[84:87], v[56:59]
	ds_read_b128 v[84:87], v37 offset:0x100
	s_waitcnt lgkmcnt(4)
	s_nop 0
	v_mfma_f32_16x16x32_f16 v[60:63], v[10:13], v[88:91], v[60:63]
	ds_read_b128 v[88:91], v37 offset:0x200
	s_waitcnt lgkmcnt(4)
	s_nop 0
	v_mfma_f32_16x16x32_f16 v[64:67], v[10:13], v[72:75], v[64:67]
	ds_read_b128 v[72:75], v37 offset:0x300
	s_waitcnt lgkmcnt(4)
	s_nop 0
	v_mfma_f32_16x16x32_f16 v[68:71], v[10:13], v[76:79], v[68:71]
	s_waitcnt lgkmcnt(3)
	s_nop 0
	v_mfma_f32_16x16x32_f16 v[56:59], v[18:21], v[80:83], v[56:59]
	s_waitcnt lgkmcnt(2)
	s_nop 0
	v_mfma_f32_16x16x32_f16 v[60:63], v[18:21], v[84:87], v[60:63]
	s_waitcnt lgkmcnt(1)
	s_nop 0
	v_mfma_f32_16x16x32_f16 v[64:67], v[18:21], v[88:91], v[64:67]
	s_waitcnt lgkmcnt(0)
	s_nop 0
	v_mfma_f32_16x16x32_f16 v[68:71], v[18:21], v[72:75], v[68:71]
	s_nop 1
	v_cvt_pk_f16_f32 v51, v58, v59
	v_pk_max_f16 v51, v51, 0
	v_cvt_pk_f16_f32 v50, v56, v57
	v_pk_max_f16 v50, v50, 0
	v_cvt_pk_f16_f32 v57, v62, v63
	v_pk_max_f16 v57, v57, 0
	v_cvt_pk_f16_f32 v56, v60, v61
	v_pk_max_f16 v56, v56, 0
	ds_write2st64_b64 v48, v[50:51], v[56:57] offset1:8
	v_cvt_pk_f16_f32 v51, v66, v67
	v_pk_max_f16 v51, v51, 0
	v_cvt_pk_f16_f32 v50, v64, v65
	v_pk_max_f16 v50, v50, 0
	v_cvt_pk_f16_f32 v57, v70, v71
	v_pk_max_f16 v57, v57, 0
	v_cvt_pk_f16_f32 v56, v68, v69
	v_pk_max_f16 v56, v56, 0
	ds_write2st64_b64 v48, v[50:51], v[56:57] offset0:16 offset1:24
	s_waitcnt lgkmcnt(0)
	s_barrier
	v_lshl_or_b32 v40, v40, 8, v29
	s_add_i32 m0, s25, 0x8000
	s_xor_b64 s[6:7], s[6:7], -1
	global_load_lds_dwordx4 v40, s[4:5]
	v_lshl_or_b32 v40, v41, 8, v31
	s_add_i32 m0, s24, 0x8000
	v_add_u32_e32 v46, s22, v46
	global_load_lds_dwordx4 v40, s[4:5]
	v_lshl_or_b32 v40, v42, 8, v29
	s_mov_b32 m0, s25
	s_nop 0
	global_load_lds_dwordx4 v40, s[4:5]
	v_lshl_or_b32 v40, v45, 8, v31
	s_mov_b32 m0, s24
	s_nop 0
	global_load_lds_dwordx4 v40, s[4:5]
	v_add_u32_e32 v40, v39, v43
	ds_read_b128 v[56:59], v40
	ds_read_b128 v[60:63], v49
	v_add_u32_e32 v40, s18, v38
	v_ashrrev_i32_e32 v41, 31, v40
	v_lshlrev_b64 v[50:51], 8, v[40:41]
	v_add_u32_e32 v40, 32, v40
	v_ashrrev_i32_e32 v41, 31, v40
	v_lshlrev_b64 v[40:41], 8, v[40:41]
	v_lshl_add_u64 v[50:51], v[0:1], 0, v[50:51]
	v_lshl_add_u64 v[40:41], v[0:1], 0, v[40:41]
	s_waitcnt lgkmcnt(0)
	global_store_dwordx4 v[50:51], v[56:59], off
	global_store_dwordx4 v[40:41], v[60:63], off
	s_add_i32 s18, s18, s21
	s_waitcnt vmcnt(8)
	s_cmp_lt_i32 s2, s13
	v_mov_b32_e32 v50, v27
	v_mov_b32_e32 v51, v92
	v_mov_b32_e32 v40, v93
	v_mov_b32_e32 v41, v94
	v_mov_b32_e32 v42, v95
	v_mov_b32_e32 v45, v96
	s_cbranch_scc0 .LBB8_8

	.amdhsa_kernel _Z10mp2_kernelILb0ELi2EEvPKDF16_PDF16_PKiPKfPKDv8_DF16_S6_S6_ii
		.amdhsa_group_segment_fixed_size 0
		.amdhsa_private_segment_fixed_size 0
		.amdhsa_kernarg_size 320
		.amdhsa_user_sgpr_count 2
		.amdhsa_user_sgpr_dispatch_ptr 0
		.amdhsa_user_sgpr_queue_ptr 0
		.amdhsa_user_sgpr_kernarg_segment_ptr 1
		.amdhsa_user_sgpr_dispatch_id 0
		.amdhsa_user_sgpr_kernarg_preload_length 0
		.amdhsa_user_sgpr_kernarg_preload_offset 0
		.amdhsa_user_sgpr_private_segment_size 0
		.amdhsa_uses_dynamic_stack 0
		.amdhsa_enable_private_segment 0
		.amdhsa_system_sgpr_workgroup_id_x 1
		.amdhsa_system_sgpr_workgroup_id_y 0
		.amdhsa_system_sgpr_workgroup_id_z 0
		.amdhsa_system_sgpr_workgroup_info 0
		.amdhsa_system_vgpr_workitem_id 0
		.amdhsa_next_free_vgpr 99
		.amdhsa_next_free_sgpr 28
		.amdhsa_accum_offset 100
		.amdhsa_reserve_vcc 1
		.amdhsa_float_round_mode_32 0
		.amdhsa_float_round_mode_16_64 0
		.amdhsa_float_denorm_mode_32 3
		.amdhsa_float_denorm_mode_16_64 3
		.amdhsa_dx10_clamp 1
		.amdhsa_ieee_mode 1
		.amdhsa_fp16_overflow 0
		.amdhsa_tg_split 0
		.amdhsa_exception_fp_ieee_invalid_op 0
		.amdhsa_exception_fp_denorm_src 0
		.amdhsa_exception_fp_ieee_div_zero 0
		.amdhsa_exception_fp_ieee_overflow 0
		.amdhsa_exception_fp_ieee_underflow 0
		.amdhsa_exception_fp_ieee_inexact 0
		.amdhsa_exception_int_div_zero 0
	.end_amdhsa_kernel

amdhsa.kernels:
  - .agpr_count:     0
    .args:
      - .actual_access:  write_only
        .address_space:  global
        .offset:         0
        .size:           8
        .value_kind:     global_buffer
      - .actual_access:  read_only
        .address_space:  global
        .offset:         8
        .size:           8
        .value_kind:     global_buffer
      - .actual_access:  read_only
        .address_space:  global
        .offset:         16
        .size:           8
        .value_kind:     global_buffer
      - .actual_access:  read_only
        .address_space:  global
        .offset:         24
        .size:           8
        .value_kind:     global_buffer
      - .actual_access:  read_only
        .address_space:  global
        .offset:         32
        .size:           8
        .value_kind:     global_buffer
      - .actual_access:  read_only
        .address_space:  global
        .offset:         40
        .size:           8
        .value_kind:     global_buffer
      - .actual_access:  read_only
        .address_space:  global
        .offset:         48
        .size:           8
        .value_kind:     global_buffer
      - .actual_access:  read_only
        .address_space:  global
        .offset:         56
        .size:           8
        .value_kind:     global_buffer
      - .actual_access:  read_only
        .address_space:  global
        .offset:         64
        .size:           8
        .value_kind:     global_buffer
      - .actual_access:  read_only
        .address_space:  global
        .offset:         72
        .size:           8
        .value_kind:     global_buffer
    .group_segment_fixed_size: 0
    .kernarg_segment_align: 8
    .kernarg_segment_size: 80
    .language:       OpenCL C
    .language_version:
      - 2
      - 0
    .max_flat_workgroup_size: 64
    .name:           _Z11prep_kernelPDv8_DF16_PKfS2_S2_S2_S2_S2_S2_S2_S2_
    .private_segment_fixed_size: 0
    .sgpr_count:     20
    .sgpr_spill_count: 0
    .symbol:         _Z11prep_kernelPDv8_DF16_PKfS2_S2_S2_S2_S2_S2_S2_S2_.kd
    .uniform_work_group_size: 1
    .uses_dynamic_stack: false
    .vgpr_count:     18
    .vgpr_spill_count: 0
    .wavefront_size: 64
  - .agpr_count:     0
    .args:
      - .actual_access:  read_only
        .address_space:  global
        .offset:         0
        .size:           8
        .value_kind:     global_buffer
      - .actual_access:  read_only
        .address_space:  global
        .offset:         8
        .size:           8
        .value_kind:     global_buffer
      - .actual_access:  write_only
        .address_space:  global
        .offset:         16
        .size:           8
        .value_kind:     global_buffer
    .group_segment_fixed_size: 0
    .kernarg_segment_align: 8
    .kernarg_segment_size: 24
    .language:       OpenCL C
    .language_version:
      - 2
      - 0
    .max_flat_workgroup_size: 256
    .name:           _Z11init_kernelPKfS0_PDF16_
    .private_segment_fixed_size: 0
    .sgpr_count:     16
    .sgpr_spill_count: 0
    .symbol:         _Z11init_kernelPKfS0_PDF16_.kd
    .uniform_work_group_size: 1
    .uses_dynamic_stack: false
    .vgpr_count:     118
    .vgpr_spill_count: 0
    .wavefront_size: 64
  - .agpr_count:     0
    .args:
      - .actual_access:  read_only
        .address_space:  global
        .offset:         0
        .size:           8
        .value_kind:     global_buffer
      - .actual_access:  write_only
        .address_space:  global
        .offset:         8
        .size:           8
        .value_kind:     global_buffer
      - .actual_access:  read_only
        .address_space:  global
        .offset:         16
        .size:           8
        .value_kind:     global_buffer
      - .actual_access:  read_only
        .address_space:  global
        .offset:         24
        .size:           8
        .value_kind:     global_buffer
      - .actual_access:  read_only
        .address_space:  global
        .offset:         32
        .size:           8
        .value_kind:     global_buffer
      - .actual_access:  read_only
        .address_space:  global
        .offset:         40
        .size:           8
        .value_kind:     global_buffer
      - .actual_access:  read_only
        .address_space:  global
        .offset:         48
        .size:           8
        .value_kind:     global_buffer
      - .offset:         56
        .size:           4
        .value_kind:     by_value
      - .offset:         64
        .size:           4
        .value_kind:     hidden_block_count_x
      - .offset:         68
        .size:           4
        .value_kind:     hidden_block_count_y
      - .offset:         72
        .size:           4
        .value_kind:     hidden_block_count_z
      - .offset:         76
        .size:           2
        .value_kind:     hidden_group_size_x
      - .offset:         78
        .size:           2
        .value_kind:     hidden_group_size_y
      - .offset:         80
        .size:           2
        .value_kind:     hidden_group_size_z
      - .offset:         82
        .size:           2
        .value_kind:     hidden_remainder_x
      - .offset:         84
        .size:           2
        .value_kind:     hidden_remainder_y
      - .offset:         86
        .size:           2
        .value_kind:     hidden_remainder_z
      - .offset:         104
        .size:           8
        .value_kind:     hidden_global_offset_x
      - .offset:         112
        .size:           8
        .value_kind:     hidden_global_offset_y
      - .offset:         120
        .size:           8
        .value_kind:     hidden_global_offset_z
      - .offset:         128
        .size:           2
        .value_kind:     hidden_grid_dims
      - .offset:         184
        .size:           4
        .value_kind:     hidden_dynamic_lds_size
    .group_segment_fixed_size: 0
    .kernarg_segment_align: 8
    .kernarg_segment_size: 320
    .language:       OpenCL C
    .language_version:
      - 2
      - 0
    .max_flat_workgroup_size: 512
    .name:           _Z12xproj_kernelPKDF16_PDF16_PKDv8_DF16_PKfS6_S6_S6_i
    .private_segment_fixed_size: 0
    .sgpr_count:     30
    .sgpr_spill_count: 0
    .symbol:         _Z12xproj_kernelPKDF16_PDF16_PKDv8_DF16_PKfS6_S6_S6_i.kd
    .uniform_work_group_size: 1
    .uses_dynamic_stack: false
    .vgpr_count:     16
    .vgpr_spill_count: 0
    .wavefront_size: 64
  - .agpr_count:     0
    .args:
      - .actual_access:  read_only
        .address_space:  global
        .offset:         0
        .size:           8
        .value_kind:     global_buffer
      - .actual_access:  read_only
        .address_space:  global
        .offset:         8
        .size:           8
        .value_kind:     global_buffer
      - .actual_access:  write_only
        .address_space:  global
        .offset:         16
        .size:           8
        .value_kind:     global_buffer
    .group_segment_fixed_size: 5120
    .kernarg_segment_align: 8
    .kernarg_segment_size: 24
    .language:       OpenCL C
    .language_version:
      - 2
      - 0
    .max_flat_workgroup_size: 1024
    .name:           _Z11lstm_kernelPKDF16_PKDv8_DF16_Pf
    .private_segment_fixed_size: 0
    .sgpr_count:     18
    .sgpr_spill_count: 0
    .symbol:         _Z11lstm_kernelPKDF16_PKDv8_DF16_Pf.kd
    .uniform_work_group_size: 1
    .uses_dynamic_stack: false
    .vgpr_count:     52
    .vgpr_spill_count: 0
    .wavefront_size: 64
  - .agpr_count:     0
    .args:
      - .actual_access:  read_only
        .address_space:  global
        .offset:         0
        .size:           8
        .value_kind:     global_buffer
      - .actual_access:  read_only
        .address_space:  global
        .offset:         8
        .size:           8
        .value_kind:     global_buffer
      - .actual_access:  write_only
        .address_space:  global
        .offset:         16
        .size:           8
        .value_kind:     global_buffer
    .group_segment_fixed_size: 36096
    .kernarg_segment_align: 8
    .kernarg_segment_size: 24
    .language:       OpenCL C
    .language_version:
      - 2
      - 0
    .max_flat_workgroup_size: 256
    .name:           _Z12lstm2_kernelPKDF16_PKDv8_DF16_Pf
    .private_segment_fixed_size: 0
    .sgpr_count:     38
    .sgpr_spill_count: 0
    .symbol:         _Z12lstm2_kernelPKDF16_PKDv8_DF16_Pf.kd
    .uniform_work_group_size: 1
    .uses_dynamic_stack: false
    .vgpr_count:     252
    .vgpr_spill_count: 0
    .wavefront_size: 64
  - .agpr_count:     0
    .args:
      - .address_space:  global
        .offset:         0
        .size:           8
        .value_kind:     global_buffer
      - .actual_access:  write_only
        .address_space:  global
        .offset:         8
        .size:           8
        .value_kind:     global_buffer
      - .address_space:  global
        .offset:         16
        .size:           8
        .value_kind:     global_buffer
      - .address_space:  global
        .offset:         24
        .size:           8
        .value_kind:     global_buffer
      - .actual_access:  read_only
        .address_space:  global
        .offset:         32
        .size:           8
        .value_kind:     global_buffer
      - .actual_access:  read_only
        .address_space:  global
        .offset:         40
        .size:           8
        .value_kind:     global_buffer
      - .actual_access:  read_only
        .address_space:  global
        .offset:         48
        .size:           8
        .value_kind:     global_buffer
      - .offset:         56
        .size:           4
        .value_kind:     by_value
      - .offset:         60
        .size:           4
        .value_kind:     by_value
      - .offset:         64
        .size:           4
        .value_kind:     hidden_block_count_x
      - .offset:         68
        .size:           4
        .value_kind:     hidden_block_count_y
      - .offset:         72
        .size:           4
        .value_kind:     hidden_block_count_z
      - .offset:         76
        .size:           2
        .value_kind:     hidden_group_size_x
      - .offset:         78
        .size:           2
        .value_kind:     hidden_group_size_y
      - .offset:         80
        .size:           2
        .value_kind:     hidden_group_size_z
      - .offset:         82
        .size:           2
        .value_kind:     hidden_remainder_x
      - .offset:         84
        .size:           2
        .value_kind:     hidden_remainder_y
      - .offset:         86
        .size:           2
        .value_kind:     hidden_remainder_z
      - .offset:         104
        .size:           8
        .value_kind:     hidden_global_offset_x
      - .offset:         112
        .size:           8
        .value_kind:     hidden_global_offset_y
      - .offset:         120
        .size:           8
        .value_kind:     hidden_global_offset_z
      - .offset:         128
        .size:           2
        .value_kind:     hidden_grid_dims
      - .offset:         184
        .size:           4
        .value_kind:     hidden_dynamic_lds_size
    .group_segment_fixed_size: 0
    .kernarg_segment_align: 8
    .kernarg_segment_size: 320
    .language:       OpenCL C
    .language_version:
      - 2
      - 0
    .max_flat_workgroup_size: 512
    .name:           _Z10mp2_kernelILb0ELi0EEvPKDF16_PDF16_PKiPKfPKDv8_DF16_S6_S6_ii
    .private_segment_fixed_size: 0
    .sgpr_count:     54
    .sgpr_spill_count: 0
    .symbol:         _Z10mp2_kernelILb0ELi0EEvPKDF16_PDF16_PKiPKfPKDv8_DF16_S6_S6_ii.kd
    .uniform_work_group_size: 1
    .uses_dynamic_stack: false
    .vgpr_count:     244
    .vgpr_spill_count: 0
    .wavefront_size: 64
  - .agpr_count:     0
    .args:
      - .actual_access:  read_only
        .address_space:  global
        .offset:         0
        .size:           8
        .value_kind:     global_buffer
      - .actual_access:  write_only
        .address_space:  global
        .offset:         8
        .size:           8
        .value_kind:     global_buffer
      - .address_space:  global
        .offset:         16
        .size:           8
        .value_kind:     global_buffer
      - .address_space:  global
        .offset:         24
        .size:           8
        .value_kind:     global_buffer
      - .actual_access:  read_only
        .address_space:  global
        .offset:         32
        .size:           8
        .value_kind:     global_buffer
      - .actual_access:  read_only
        .address_space:  global
        .offset:         40
        .size:           8
        .value_kind:     global_buffer
      - .actual_access:  read_only
        .address_space:  global
        .offset:         48
        .size:           8
        .value_kind:     global_buffer
      - .offset:         56
        .size:           4
        .value_kind:     by_value
      - .offset:         60
        .size:           4
        .value_kind:     by_value
      - .offset:         64
        .size:           4
        .value_kind:     hidden_block_count_x
      - .offset:         68
        .size:           4
        .value_kind:     hidden_block_count_y
      - .offset:         72
        .size:           4
        .value_kind:     hidden_block_count_z
      - .offset:         76
        .size:           2
        .value_kind:     hidden_group_size_x
      - .offset:         78
        .size:           2
        .value_kind:     hidden_group_size_y
      - .offset:         80
        .size:           2
        .value_kind:     hidden_group_size_z
      - .offset:         82
        .size:           2
        .value_kind:     hidden_remainder_x
      - .offset:         84
        .size:           2
        .value_kind:     hidden_remainder_y
      - .offset:         86
        .size:           2
        .value_kind:     hidden_remainder_z
      - .offset:         104
        .size:           8
        .value_kind:     hidden_global_offset_x
      - .offset:         112
        .size:           8
        .value_kind:     hidden_global_offset_y
      - .offset:         120
        .size:           8
        .value_kind:     hidden_global_offset_z
      - .offset:         128
        .size:           2
        .value_kind:     hidden_grid_dims
      - .offset:         184
        .size:           4
        .value_kind:     hidden_dynamic_lds_size
    .group_segment_fixed_size: 0
    .kernarg_segment_align: 8
    .kernarg_segment_size: 320
    .language:       OpenCL C
    .language_version:
      - 2
      - 0
    .max_flat_workgroup_size: 512
    .name:           _Z10mp2_kernelILb0ELi1EEvPKDF16_PDF16_PKiPKfPKDv8_DF16_S6_S6_ii
    .private_segment_fixed_size: 0
    .sgpr_count:     30
    .sgpr_spill_count: 0
    .symbol:         _Z10mp2_kernelILb0ELi1EEvPKDF16_PDF16_PKiPKfPKDv8_DF16_S6_S6_ii.kd
    .uniform_work_group_size: 1
    .uses_dynamic_stack: false
    .vgpr_count:     234
    .vgpr_spill_count: 0
    .wavefront_size: 64
  - .agpr_count:     0
    .args:
      - .address_space:  global
        .offset:         0
        .size:           8
        .value_kind:     global_buffer
      - .actual_access:  write_only
        .address_space:  global
        .offset:         8
        .size:           8
        .value_kind:     global_buffer
      - .actual_access:  read_only
        .address_space:  global
        .offset:         16
        .size:           8
        .value_kind:     global_buffer
      - .actual_access:  read_only
        .address_space:  global
        .offset:         24
        .size:           8
        .value_kind:     global_buffer
      - .actual_access:  read_only
        .address_space:  global
        .offset:         32
        .size:           8
        .value_kind:     global_buffer
      - .actual_access:  read_only
        .address_space:  global
        .offset:         40
        .size:           8
        .value_kind:     global_buffer
      - .actual_access:  read_only
        .address_space:  global
        .offset:         48
        .size:           8
        .value_kind:     global_buffer
      - .offset:         56
        .size:           4
        .value_kind:     by_value
      - .offset:         60
        .size:           4
        .value_kind:     by_value
      - .offset:         64
        .size:           4
        .value_kind:     hidden_block_count_x
      - .offset:         68
        .size:           4
        .value_kind:     hidden_block_count_y
      - .offset:         72
        .size:           4
        .value_kind:     hidden_block_count_z
      - .offset:         76
        .size:           2
        .value_kind:     hidden_group_size_x
      - .offset:         78
        .size:           2
        .value_kind:     hidden_group_size_y
      - .offset:         80
        .size:           2
        .value_kind:     hidden_group_size_z
      - .offset:         82
        .size:           2
        .value_kind:     hidden_remainder_x
      - .offset:         84
        .size:           2
        .value_kind:     hidden_remainder_y
      - .offset:         86
        .size:           2
        .value_kind:     hidden_remainder_z
      - .offset:         104
        .size:           8
        .value_kind:     hidden_global_offset_x
      - .offset:         112
        .size:           8
        .value_kind:     hidden_global_offset_y
      - .offset:         120
        .size:           8
        .value_kind:     hidden_global_offset_z
      - .offset:         128
        .size:           2
        .value_kind:     hidden_grid_dims
      - .offset:         184
        .size:           4
        .value_kind:     hidden_dynamic_lds_size
    .group_segment_fixed_size: 0
    .kernarg_segment_align: 8
    .kernarg_segment_size: 320
    .language:       OpenCL C
    .language_version:
      - 2
      - 0
    .max_flat_workgroup_size: 512
    .name:           _Z9mp_kernelILi1EEvPKDF16_PDF16_PKiPKfPKDv8_DF16_S6_S6_ii
    .private_segment_fixed_size: 0
    .sgpr_count:     46
    .sgpr_spill_count: 0
    .symbol:         _Z9mp_kernelILi1EEvPKDF16_PDF16_PKiPKfPKDv8_DF16_S6_S6_ii.kd
    .uniform_work_group_size: 1
    .uses_dynamic_stack: false
    .vgpr_count:     70
    .vgpr_spill_count: 0
    .wavefront_size: 64
  - .agpr_count:     0
    .args:
      - .address_space:  global
        .offset:         0
        .size:           8
        .value_kind:     global_buffer
      - .actual_access:  write_only
        .address_space:  global
        .offset:         8
        .size:           8
        .value_kind:     global_buffer
      - .address_space:  global
        .offset:         16
        .size:           8
        .value_kind:     global_buffer
      - .address_space:  global
        .offset:         24
        .size:           8
        .value_kind:     global_buffer
      - .actual_access:  read_only
        .address_space:  global
        .offset:         32
        .size:           8
        .value_kind:     global_buffer
      - .actual_access:  read_only
        .address_space:  global
        .offset:         40
        .size:           8
        .value_kind:     global_buffer
      - .actual_access:  read_only
        .address_space:  global
        .offset:         48
        .size:           8
        .value_kind:     global_buffer
      - .offset:         56
        .size:           4
        .value_kind:     by_value
      - .offset:         60
        .size:           4
        .value_kind:     by_value
      - .offset:         64
        .size:           4
        .value_kind:     hidden_block_count_x
      - .offset:         68
        .size:           4
        .value_kind:     hidden_block_count_y
      - .offset:         72
        .size:           4
        .value_kind:     hidden_block_count_z
      - .offset:         76
        .size:           2
        .value_kind:     hidden_group_size_x
      - .offset:         78
        .size:           2
        .value_kind:     hidden_group_size_y
      - .offset:         80
        .size:           2
        .value_kind:     hidden_group_size_z
      - .offset:         82
        .size:           2
        .value_kind:     hidden_remainder_x
      - .offset:         84
        .size:           2
        .value_kind:     hidden_remainder_y
      - .offset:         86
        .size:           2
        .value_kind:     hidden_remainder_z
      - .offset:         104
        .size:           8
        .value_kind:     hidden_global_offset_x
      - .offset:         112
        .size:           8
        .value_kind:     hidden_global_offset_y
      - .offset:         120
        .size:           8
        .value_kind:     hidden_global_offset_z
      - .offset:         128
        .size:           2
        .value_kind:     hidden_grid_dims
      - .offset:         184
        .size:           4
        .value_kind:     hidden_dynamic_lds_size
    .group_segment_fixed_size: 0
    .kernarg_segment_align: 8
    .kernarg_segment_size: 320
    .language:       OpenCL C
    .language_version:
      - 2
      - 0
    .max_flat_workgroup_size: 512
    .name:           _Z10mp2_kernelILb0ELi2EEvPKDF16_PDF16_PKiPKfPKDv8_DF16_S6_S6_ii
    .private_segment_fixed_size: 0
    .sgpr_count:     34
    .sgpr_spill_count: 0
    .symbol:         _Z10mp2_kernelILb0ELi2EEvPKDF16_PDF16_PKiPKfPKDv8_DF16_S6_S6_ii.kd
    .uniform_work_group_size: 1
    .uses_dynamic_stack: false
    .vgpr_count:     99
    .vgpr_spill_count: 0
    .wavefront_size: 64
